# speedup vs baseline: 1.0400x; 1.0374x over previous
.Lmy_nonp6:
	s_and_b64 vcc, exec, s[30:31]
	s_cbranch_vccz .LBB1_43
	s_waitcnt vmcnt(0)
	s_load_dwordx2 s[0:1], s[0:1], 0x68
	v_mov_b32_e32 v99, 0
	v_lshl_or_b32 v65, s42, 1, v115
	s_waitcnt lgkmcnt(0)
	s_add_u32 s8, s0, s33
	s_addc_u32 s9, s1, 0
	global_load_dwordx4 v[2:5], v98, s[8:9]
	s_movk_i32 s0, 0x1000
	v_lshl_add_u64 v[66:67], s[8:9], 0, v[98:99]
	v_add_co_u32_e32 v10, vcc, s0, v66
	v_cmp_gt_u32_e64 s[0:1], 21, v114
	s_nop 0
	v_addc_co_u32_e32 v11, vcc, 0, v67, vcc
	global_load_dwordx4 v[6:9], v[10:11], off offset:2048
	global_load_dwordx4 v[34:37], v[10:11], off
	global_load_dwordx4 v[54:57], v[10:11], off offset:3072
	v_cndmask_b32_e64 v64, 20, v114, s[0:1]
	s_movk_i32 s7, 0x150
	v_lshlrev_b32_e32 v71, 4, v65
	v_mad_u64_u32 v[12:13], s[12:13], v65, s7, v[64:65]
	v_mov_b32_e32 v13, v99
	v_or_b32_e32 v70, 1, v71
	v_lshlrev_b64 v[12:13], 2, v[12:13]
	v_mad_u64_u32 v[86:87], s[12:13], v70, 21, v[64:65]
	v_lshlrev_b32_e32 v73, 2, v64
	v_lshl_add_u64 v[14:15], s[50:51], 0, v[12:13]
	v_lshl_add_u64 v[12:13], s[36:37], 0, v[12:13]
	v_mov_b32_e32 v87, v99
	global_load_dword v81, v73, s[44:45]
	global_load_dword v62, v73, s[46:47]
	global_load_dword v83, v73, s[48:49]
	global_load_dword v69, v73, s[38:39]
	global_load_dword v63, v73, s[40:41]
	global_load_dword v75, v[14:15], off
	global_load_dword v72, v[12:13], off
	v_lshlrev_b64 v[12:13], 2, v[86:87]
	v_lshl_add_u64 v[14:15], s[50:51], 0, v[12:13]
	v_lshl_add_u64 v[12:13], s[36:37], 0, v[12:13]
	global_load_dwordx4 v[50:53], v98, s[8:9] offset:1024
	global_load_dword v76, v[14:15], off
	global_load_dword v74, v[12:13], off
	global_load_dwordx4 v[58:61], v[10:11], off offset:1024
	global_load_dwordx4 v[118:121], v[66:67], off offset:2048
	global_load_dwordx4 v[122:125], v[66:67], off offset:3072
	v_add_u32_e32 v98, 21, v86
	v_lshlrev_b64 v[12:13], 2, v[98:99]
	v_lshl_add_u64 v[10:11], s[50:51], 0, v[12:13]
	v_lshl_add_u64 v[12:13], s[36:37], 0, v[12:13]
	global_load_dword v105, v[10:11], off
	global_load_dword v77, v[12:13], off
	v_add_u32_e32 v98, 42, v86
	v_lshlrev_b64 v[14:15], 2, v[98:99]
	v_lshl_add_u64 v[10:11], s[50:51], 0, v[14:15]
	v_lshl_add_u64 v[12:13], s[36:37], 0, v[14:15]
	global_load_dword v106, v[10:11], off
	global_load_dword v78, v[12:13], off
	v_add_u32_e32 v98, 63, v86
	v_lshlrev_b64 v[14:15], 2, v[98:99]
	v_lshl_add_u64 v[10:11], s[50:51], 0, v[14:15]
	v_lshl_add_u64 v[12:13], s[36:37], 0, v[14:15]
	global_load_dword v107, v[10:11], off
	global_load_dword v79, v[12:13], off
	v_add_u32_e32 v98, 0x54, v86
	v_or_b32_e32 v68, 10, v71
	v_lshlrev_b64 v[126:127], 2, v[98:99]
	v_lshl_add_u64 v[42:43], s[50:51], 0, v[126:127]
	v_lshl_add_u64 v[44:45], s[36:37], 0, v[126:127]
	global_load_dword v108, v[42:43], off
	global_load_dword v102, v[44:45], off
	v_add_u32_e32 v98, 0x69, v86
	v_lshlrev_b64 v[46:47], 2, v[98:99]
	v_lshl_add_u64 v[84:85], s[50:51], 0, v[46:47]
	v_lshl_add_u64 v[88:89], s[36:37], 0, v[46:47]
	global_load_dword v109, v[84:85], off
	global_load_dword v103, v[88:89], off
	v_add_u32_e32 v98, 0x7e, v86
	v_lshlrev_b64 v[90:91], 2, v[98:99]
	v_lshl_add_u64 v[84:85], s[50:51], 0, v[90:91]
	v_lshl_add_u64 v[88:89], s[36:37], 0, v[90:91]
	global_load_dword v104, v[84:85], off
	global_load_dword v101, v[88:89], off
	v_add_u32_e32 v98, 0x93, v86
	v_lshlrev_b64 v[90:91], 2, v[98:99]
	v_add_u32_e32 v98, 0xa8, v86
	v_lshl_add_u64 v[42:43], s[50:51], 0, v[90:91]
	global_load_dword v100, v[42:43], off
	v_lshl_add_u64 v[42:43], s[36:37], 0, v[90:91]
	global_load_dword v84, v[42:43], off
	v_lshlrev_b64 v[42:43], 2, v[98:99]
	v_lshl_add_u64 v[44:45], s[50:51], 0, v[42:43]
	global_load_dword v98, v[44:45], off
	v_lshl_add_u64 v[42:43], s[36:37], 0, v[42:43]
	global_load_dword v85, v[42:43], off
	v_min_u32_e32 v42, 0x79, v68
	v_mul_u32_u24_e32 v42, 21, v42
	v_add_lshl_u32 v42, v42, v64, 2
	v_or_b32_e32 v43, 11, v71
	global_load_dword v97, v42, s[50:51]
	global_load_dword v86, v42, s[36:37]
	v_min_u32_e32 v42, 0x79, v43
	v_mul_u32_u24_e32 v42, 21, v42
	v_add_lshl_u32 v42, v42, v64, 2
	v_or_b32_e32 v44, 12, v71
	global_load_dword v96, v42, s[50:51]
	global_load_dword v87, v42, s[36:37]
	v_min_u32_e32 v42, 0x79, v44
	v_mul_u32_u24_e32 v42, 21, v42
	v_add_lshl_u32 v42, v42, v64, 2
	v_or_b32_e32 v45, 13, v71
	global_load_dword v95, v42, s[50:51]
	global_load_dword v92, v42, s[36:37]
	v_min_u32_e32 v42, 0x79, v45
	v_mul_u32_u24_e32 v42, 21, v42
	v_add_lshl_u32 v42, v42, v64, 2
	global_load_dword v93, v42, s[50:51]
	global_load_dword v89, v42, s[36:37]
	v_or_b32_e32 v42, 14, v71
	v_or_b32_e32 v46, 15, v71
	v_min_u32_e32 v80, 0x79, v42
	v_min_u32_e32 v47, 0x79, v46
	v_mul_u32_u24_e32 v80, 21, v80
	v_mul_u32_u24_e32 v47, 21, v47
	v_add_lshl_u32 v80, v80, v64, 2
	v_add_lshl_u32 v47, v47, v64, 2
	global_load_dword v94, v80, s[50:51]
	global_load_dword v90, v80, s[36:37]
	global_load_dword v91, v47, s[50:51]
	global_load_dword v88, v47, s[36:37]
	s_branch .LBB1_43
.LBB1_46:
	v_lshlrev_b32_e32 v39, 2, v0
	s_mov_b64 exec, 0x1fffff
	global_load_dword v40, v39, s[24:25]
	global_load_dword v41, v39, s[52:53]
	global_load_dword v44, v39, s[58:59]
	global_load_dword v12, v39, s[30:31]
	global_load_dword v13, v39, s[10:11]
	global_load_dword v27, v39, s[42:43]
	global_load_dword v28, v39, s[12:13]
	global_load_dword v29, v39, s[54:55]
	global_load_dword v30, v39, s[56:57]
	global_load_dword v31, v39, s[60:61]
	s_mov_b64 exec, 0xff
	global_load_dword v36, v39, s[16:17]
	s_mov_b64 exec, -1
	global_load_dword v37, v39, s[14:15]
	global_load_dword v38, v39, s[18:19]
	v_add_u32_e32 v1, 0xf550, v98
	s_waitcnt vmcnt(15)
	v_mov_b32_e32 v3, v6
	s_waitcnt vmcnt(14)
	v_mov_b32_e32 v4, v10
	s_waitcnt vmcnt(13)
	v_mov_b32_e32 v5, v14
	ds_write_b128 v98, v[86:89] offset:62800
	ds_write_b128 v98, v[62:65] offset:63824
	ds_write_b128 v98, v[58:61] offset:64848
	ds_write_b128 v1, v[54:57] offset:3072
	ds_write_b128 v1, v[50:53] offset:4096
	ds_write_b128 v1, v[2:5] offset:5120
	v_cmp_gt_u32_e64 s[4:5], 21, v0
	v_lshlrev_b32_e32 v1, 2, v0
	s_and_saveexec_b64 s[64:65], s[4:5]
	s_cbranch_execz .LBB1_6
.LBB1_47:
	s_mov_b32 s10, 0x800000
	v_add_u32_e32 v32, 0x12ff0, v1
	v_add_u32_e32 v33, 0x12f30, v1
	v_add_u32_e32 v34, 0x12ed0, v1
	v_add_u32_e32 v35, 0x11d50, v1
	s_waitcnt vmcnt(9)
	ds_write_b32 v33, v12
	s_waitcnt vmcnt(8)
	ds_write_b32 v34, v13
	s_waitcnt vmcnt(6)
	ds_write2_b32 v35, v27, v28 offset1:21
	v_add_f32_e32 v3, 0x3727c5ac, v40
	v_sub_f32_e32 v4, v41, v44
	v_mul_f32_e32 v5, 0x4b800000, v3
	v_cmp_gt_f32_e32 vcc, s10, v3
	s_nop 1
	v_cndmask_b32_e32 v3, v3, v5, vcc
	v_rsq_f32_e32 v3, v3
	s_nop 0
	v_mul_f32_e32 v5, 0x45800000, v3
	v_cndmask_b32_e32 v3, v3, v5, vcc
	s_waitcnt vmcnt(5)
	v_mul_f32_e32 v3, v29, v3
	s_waitcnt vmcnt(4)
	v_fmac_f32_e32 v30, v4, v3
	ds_write_b32 v32, v30
	s_waitcnt vmcnt(3)
	ds_write_b32 v35, v31 offset:200
	s_or_b64 exec, exec, s[64:65]
	v_cmp_gt_u32_e64 s[10:11], 8, v0
	s_and_saveexec_b64 s[12:13], s[10:11]
	v_add_u32_e32 v4, 0x11df8, v1
	s_waitcnt vmcnt(2)
	ds_write_b32 v4, v36
	s_or_b64 exec, exec, s[12:13]
	v_add_u32_e32 v5, 0x11d50, v1
	s_waitcnt vmcnt(0)
	ds_write2_b32 v5, v37, v38 offset0:71 offset1:239
	s_mov_b64 s[12:13], -1
	s_branch .LBB1_10

.LBB1_55:
	v_lshrrev_b32_e32 v12, 1, v0
	v_and_b32_e32 v13, 3, v0
	v_and_or_b32 v17, v12, 12, v13
	v_and_b32_e32 v16, 16, v1
	s_lshl_b32 s7, s42, 5
	s_movk_i32 s6, 0x50
	v_or3_b32 v16, v17, v16, s7
	v_mul_lo_u32 v14, v16, s6
	v_add_u32_e32 v16, 0xf550, v14
	v_add_u32_e32 v82, v16, v116
	ds_read_b128 v[38:41], v82
	ds_read_b128 v[110:113], v82 offset:32
	s_movk_i32 s7, 0x500
	s_waitcnt vmcnt(0) lgkmcnt(1)
	v_mfma_f32_32x32x16_f16 v[18:33], v[38:41], v[2:5], 0
	v_mfma_f32_32x32x16_f16 v[2:17], v[38:41], v[6:9], 0
	s_waitcnt lgkmcnt(0)
	v_mfma_f32_32x32x16_f16 v[2:17], v[110:113], v[54:57], v[2:17]
	v_mfma_f32_32x32x16_f16 v[34:49], v[38:41], v[34:37], 0
	v_mfma_f32_32x32x16_f16 v[34:49], v[110:113], v[58:61], v[34:49]
	v_mfma_f32_32x32x16_f16 v[18:33], v[110:113], v[50:53], v[18:33]
	s_nop 5
	v_or_b32_e32 v57, 11, v71
	v_or_b32_e32 v56, 12, v71
	v_or_b32_e32 v55, 13, v71
	v_or_b32_e32 v54, 14, v71
	v_or_b32_e32 v50, 15, v71
	v_add_f32_e32 v34, v83, v34
	v_add_f32_e32 v34, v34, v75
	v_mul_f32_e32 v34, 0xbfb8aa3b, v34
	v_exp_f32_e32 v34, v34
	v_mov_b32_e32 v51, 0xf550
	v_add_f32_e32 v35, v83, v35
	v_lshl_add_u32 v51, v64, 1, v51
	v_mul_lo_u32 v52, v65, s7
	v_add_f32_e32 v35, v35, v76
	v_add_u32_e32 v80, v51, v52
	v_mul_lo_u32 v52, v70, s6
	v_add_f32_e32 v34, 1.0, v34
	v_mul_f32_e32 v35, 0xbfb8aa3b, v35
	v_add_u32_e32 v75, v51, v52
	v_add_u32_e32 v52, 0x1e0, v52
	v_rcp_f32_e32 v34, v34
	v_exp_f32_e32 v76, v35
	v_add_u32_e32 v51, v51, v52
	ds_read_u16 v52, v80
	ds_read_u16 v53, v75
	ds_read_u16 v58, v75 offset:80
	ds_read_u16 v59, v75 offset:160
	ds_read_u16 v60, v75 offset:240
	ds_read_u16 v61, v75 offset:320
	ds_read_u16 v110, v75 offset:400
	ds_read_u16 v111, v51
	s_waitcnt lgkmcnt(7)
	v_cvt_f32_f16_e32 v52, v52
	v_add_f32_e32 v18, v81, v18
	v_add_f32_e32 v36, v83, v36
	v_mul_f32_e32 v35, v72, v34
	v_mul_f32_e32 v18, v18, v34
	v_add_f32_e32 v34, 1.0, v76
	s_waitcnt vmcnt(27)
	v_add_f32_e32 v36, v36, v105
	v_rcp_f32_e32 v34, v34
	v_mul_f32_e32 v36, 0xbfb8aa3b, v36
	v_mul_f32_e32 v52, v18, v52
	s_waitcnt lgkmcnt(6)
	v_cvt_f32_f16_e32 v18, v53
	v_exp_f32_e32 v36, v36
	v_add_f32_e32 v19, v81, v19
	v_mul_f32_e32 v19, v19, v34
	v_mul_f32_e32 v53, v19, v18
	v_add_f32_e32 v18, 1.0, v36
	v_rcp_f32_e32 v18, v18
	v_add_f32_e32 v36, v83, v37
	s_waitcnt lgkmcnt(5)
	v_cvt_f32_f16_e32 v19, v58
	s_waitcnt vmcnt(25)
	v_add_f32_e32 v36, v36, v106
	v_mul_f32_e32 v36, 0xbfb8aa3b, v36
	v_exp_f32_e32 v36, v36
	v_add_f32_e32 v20, v81, v20
	v_fmac_f32_e32 v52, 0, v35
	v_mul_f32_e32 v72, v74, v34
	v_mul_f32_e32 v34, v77, v18
	v_mul_f32_e32 v18, v20, v18
	v_fmac_f32_e32 v53, v52, v72
	v_mul_f32_e32 v76, v35, v72
	v_mul_f32_e32 v58, v18, v19
	v_fmac_f32_e32 v58, v53, v34
	v_mul_f32_e32 v37, v76, v34
	v_add_f32_e32 v34, v83, v38
	v_add_f32_e32 v18, 1.0, v36
	s_waitcnt vmcnt(23)
	v_add_f32_e32 v34, v34, v107
	v_rcp_f32_e32 v18, v18
	v_mul_f32_e32 v34, 0xbfb8aa3b, v34
	s_waitcnt lgkmcnt(4)
	v_cvt_f32_f16_e32 v19, v59
	v_exp_f32_e32 v34, v34
	v_add_f32_e32 v21, v81, v21
	v_mul_f32_e32 v20, v78, v18
	v_mul_f32_e32 v18, v21, v18
	v_add_f32_e32 v21, v83, v39
	v_mul_f32_e32 v59, v18, v19
	v_add_f32_e32 v18, 1.0, v34
	s_waitcnt vmcnt(21)
	v_add_f32_e32 v21, v21, v108
	v_rcp_f32_e32 v18, v18
	v_mul_f32_e32 v21, 0xbfb8aa3b, v21
	s_waitcnt lgkmcnt(3)
	v_cvt_f32_f16_e32 v19, v60
	v_exp_f32_e32 v21, v21
	v_add_f32_e32 v22, v81, v22
	v_fmac_f32_e32 v59, v58, v20
	v_mul_f32_e32 v77, v37, v20
	v_mul_f32_e32 v20, v79, v18
	v_mul_f32_e32 v18, v22, v18
	v_mul_f32_e32 v60, v18, v19
	v_add_f32_e32 v18, 1.0, v21
	v_add_f32_e32 v21, v83, v40
	s_waitcnt vmcnt(19)
	v_add_f32_e32 v21, v21, v109
	v_rcp_f32_e32 v18, v18
	v_mul_f32_e32 v21, 0xbfb8aa3b, v21
	s_waitcnt lgkmcnt(2)
	v_cvt_f32_f16_e32 v19, v61
	v_exp_f32_e32 v21, v21
	v_add_f32_e32 v22, v81, v23
	v_fmac_f32_e32 v60, v59, v20
	v_mul_f32_e32 v39, v77, v20
	v_mul_f32_e32 v20, v102, v18
	v_mul_f32_e32 v18, v22, v18
	v_mul_f32_e32 v61, v18, v19
	v_add_f32_e32 v18, 1.0, v21
	v_add_f32_e32 v21, v83, v41
	s_waitcnt vmcnt(17)
	v_add_f32_e32 v21, v21, v104
	v_rcp_f32_e32 v18, v18
	v_mul_f32_e32 v21, 0xbfb8aa3b, v21
	s_waitcnt lgkmcnt(1)
	v_cvt_f32_f16_e32 v19, v110
	v_exp_f32_e32 v21, v21
	v_add_f32_e32 v22, v81, v24
	v_fmac_f32_e32 v61, v60, v20
	v_mul_f32_e32 v78, v39, v20
	v_mul_f32_e32 v20, v103, v18
	v_mul_f32_e32 v18, v22, v18
	v_mul_f32_e32 v72, v18, v19
	v_add_f32_e32 v18, 1.0, v21
	v_rcp_f32_e32 v18, v18
	v_add_f32_e32 v21, v81, v25
	v_fmac_f32_e32 v72, v61, v20
	v_mul_f32_e32 v79, v78, v20
	s_waitcnt vmcnt(16)
	v_mul_f32_e32 v20, v101, v18
	v_mul_f32_e32 v18, v21, v18
	v_add_f32_e32 v21, v83, v42
	s_waitcnt vmcnt(15)
	v_add_f32_e32 v21, v21, v100
	v_mul_f32_e32 v21, 0xbfb8aa3b, v21
	s_waitcnt lgkmcnt(0)
	v_cvt_f32_f16_e32 v19, v111
	v_exp_f32_e32 v21, v21
	v_add_f32_e32 v36, v83, v43
	v_mul_f32_e32 v41, v79, v20
	v_mul_f32_e32 v74, v18, v19
	v_add_f32_e32 v18, 1.0, v21
	v_fmac_f32_e32 v74, v72, v20
	v_rcp_f32_e32 v18, v18
	ds_read_u16 v19, v51 offset:80
	ds_read_u16 v20, v51 offset:160
	ds_read_u16 v21, v51 offset:240
	ds_read_u16 v22, v51 offset:320
	ds_read_u16 v23, v51 offset:400
	ds_read_u16 v24, v51 offset:480
	ds_read_u16 v25, v51 offset:560
	ds_read_u16 v42, v51 offset:640
	s_waitcnt vmcnt(13)
	v_add_f32_e32 v36, v36, v98
	s_waitcnt lgkmcnt(7)
	v_cvt_f32_f16_e32 v19, v19
	v_mul_f32_e32 v36, 0xbfb8aa3b, v36
	v_exp_f32_e32 v36, v36
	v_add_f32_e32 v26, v81, v26
	v_mul_f32_e32 v34, v84, v18
	v_mul_f32_e32 v18, v26, v18
	v_mul_f32_e32 v26, v18, v19
	v_add_f32_e32 v18, 1.0, v36
	v_fmac_f32_e32 v26, v74, v34
	v_mul_f32_e32 v84, v41, v34
	v_add_f32_e32 v34, v83, v44
	v_rcp_f32_e32 v18, v18
	s_waitcnt vmcnt(11)
	v_add_f32_e32 v34, v34, v97
	s_waitcnt lgkmcnt(6)
	v_cvt_f32_f16_e32 v19, v20
	v_mul_f32_e32 v34, 0xbfb8aa3b, v34
	v_exp_f32_e32 v36, v34
	v_add_f32_e32 v27, v81, v27
	v_mul_f32_e32 v20, v85, v18
	v_mul_f32_e32 v18, v27, v18
	v_mul_f32_e32 v34, v18, v19
	s_waitcnt lgkmcnt(5)
	v_cvt_f32_f16_e32 v19, v21
	v_add_f32_e32 v21, v83, v45
	v_add_f32_e32 v18, 1.0, v36
	s_waitcnt vmcnt(9)
	v_add_f32_e32 v21, v21, v96
	v_rcp_f32_e32 v18, v18
	v_mul_f32_e32 v21, 0xbfb8aa3b, v21
	v_exp_f32_e32 v21, v21
	v_add_f32_e32 v27, v81, v28
	v_fmac_f32_e32 v34, v26, v20
	v_mul_f32_e32 v85, v84, v20
	v_mul_f32_e32 v20, v86, v18
	v_mul_f32_e32 v18, v27, v18
	v_mul_f32_e32 v28, v18, v19
	v_add_f32_e32 v18, 1.0, v21
	v_add_f32_e32 v21, v83, v46
	s_waitcnt vmcnt(7)
	v_add_f32_e32 v21, v21, v95
	v_rcp_f32_e32 v18, v18
	v_mul_f32_e32 v21, 0xbfb8aa3b, v21
	s_waitcnt lgkmcnt(4)
	v_cvt_f32_f16_e32 v19, v22
	v_exp_f32_e32 v21, v21
	v_add_f32_e32 v22, v81, v29
	v_fmac_f32_e32 v28, v34, v20
	v_mul_f32_e32 v86, v85, v20
	v_mul_f32_e32 v20, v87, v18
	v_mul_f32_e32 v18, v22, v18
	v_mul_f32_e32 v36, v18, v19
	v_add_f32_e32 v18, 1.0, v21
	v_add_f32_e32 v21, v83, v47
	s_waitcnt vmcnt(5)
	v_add_f32_e32 v21, v21, v93
	v_rcp_f32_e32 v18, v18
	v_mul_f32_e32 v21, 0xbfb8aa3b, v21
	s_waitcnt lgkmcnt(3)
	v_cvt_f32_f16_e32 v19, v23
	v_exp_f32_e32 v21, v21
	v_add_f32_e32 v22, v81, v30
	v_fmac_f32_e32 v36, v28, v20
	v_mul_f32_e32 v87, v86, v20
	v_mul_f32_e32 v20, v92, v18
	v_mul_f32_e32 v18, v22, v18
	v_mul_f32_e32 v38, v18, v19
	v_add_f32_e32 v18, 1.0, v21
	v_add_f32_e32 v21, v83, v48
	s_waitcnt vmcnt(3)
	v_add_f32_e32 v21, v21, v94
	v_rcp_f32_e32 v18, v18
	v_mul_f32_e32 v21, 0xbfb8aa3b, v21
	s_waitcnt lgkmcnt(2)
	v_cvt_f32_f16_e32 v19, v24
	v_exp_f32_e32 v21, v21
	v_add_f32_e32 v22, v81, v31
	v_fmac_f32_e32 v38, v36, v20
	v_mul_f32_e32 v47, v87, v20
	v_mul_f32_e32 v20, v89, v18
	v_mul_f32_e32 v18, v22, v18
	v_mul_f32_e32 v40, v18, v19
	v_add_f32_e32 v18, 1.0, v21
	v_add_f32_e32 v21, v83, v49
	s_waitcnt vmcnt(1)
	v_add_f32_e32 v21, v21, v91
	v_rcp_f32_e32 v18, v18
	v_mul_f32_e32 v21, 0xbfb8aa3b, v21
	s_waitcnt lgkmcnt(1)
	v_cvt_f32_f16_e32 v19, v25
	v_exp_f32_e32 v21, v21
	v_add_f32_e32 v22, v81, v32
	v_fmac_f32_e32 v40, v38, v20
	v_mul_f32_e32 v31, v47, v20
	v_mul_f32_e32 v20, v90, v18
	v_mul_f32_e32 v18, v22, v18
	v_mul_f32_e32 v32, v18, v19
	v_add_f32_e32 v18, 1.0, v21
	v_rcp_f32_e32 v18, v18
	s_waitcnt lgkmcnt(0)
	v_cvt_f32_f16_e32 v19, v42
	v_add_f32_e32 v21, v81, v33
	v_fmac_f32_e32 v32, v40, v20
	v_mul_f32_e32 v48, v31, v20
	s_waitcnt vmcnt(0)
	v_mul_f32_e32 v20, v88, v18
	v_mul_f32_e32 v18, v21, v18
	v_mul_f32_e32 v30, v18, v19
	v_fmac_f32_e32 v30, v32, v20
	v_mul_f32_e32 v49, v48, v20
	s_and_saveexec_b64 s[6:7], s[0:1]
	s_cbranch_execz .LBB1_57
	v_add_f32_e32 v2, 0, v2
	v_add_f32_e32 v2, v2, v3
	v_add_f32_e32 v2, v2, v4
	v_add_f32_e32 v2, v2, v5
	v_add_f32_e32 v2, v2, v6
	v_add_f32_e32 v2, v2, v7
	v_add_f32_e32 v2, v2, v8
	v_add_f32_e32 v2, v2, v9
	v_add_f32_e32 v2, v2, v10
	v_add_f32_e32 v2, v2, v11
	v_add_f32_e32 v2, v2, v12
	v_add_f32_e32 v2, v2, v13
	v_add_f32_e32 v2, v2, v14
	v_mul_lo_u32 v3, v65, 21
	v_add_f32_e32 v2, v2, v15
	v_add_lshl_u32 v3, v3, v114, 2
	v_add_f32_e32 v2, v2, v16
	v_add_u32_e32 v4, 0x12450, v3
	v_add_f32_e32 v2, v2, v17
	ds_write_b32 v4, v49
	v_add_u32_e32 v4, 0x126f0, v3
	v_add_u32_e32 v3, 0x12990, v3
	ds_write_b32 v4, v30
	ds_write_b32 v3, v2
.LBB1_57:
	s_or_b64 exec, exec, s[6:7]
	s_waitcnt lgkmcnt(0)
	s_barrier
	ds_read_b128 v[6:9], v82
	ds_read_b128 v[22:25], v82 offset:32
	v_cmp_ne_u32_e32 vcc, 0, v65
	s_waitcnt vmcnt(1) lgkmcnt(1)
	v_mfma_f32_32x32x16_f16 v[2:17], v[6:9], v[118:121], 0
	s_and_saveexec_b64 s[6:7], vcc
	s_cbranch_execz .LBB1_59
	v_add_u32_e32 v27, 0x12450, v73
	v_add_u32_e32 v29, 0x126f0, v73
	ds_read_b32 v99, v29
	ds_read_b32 v27, v27
	s_waitcnt lgkmcnt(0)
	v_fmac_f32_e32 v99, 0, v27

.LBB1_66:
	s_or_b64 exec, exec, s[6:7]
	s_waitcnt vmcnt(0) lgkmcnt(6)
	v_mfma_f32_32x32x16_f16 v[2:17], v[22:25], v[122:125], v[2:17]
	s_and_saveexec_b64 s[6:7], s[0:1]
	s_cbranch_execz .LBB1_68
	s_waitcnt lgkmcnt(5)
	v_add_f32_e32 v18, 0, v29
	s_waitcnt lgkmcnt(4)
	v_add_f32_e32 v18, v18, v33
	s_waitcnt lgkmcnt(3)
	v_add_f32_e32 v18, v18, v42
	v_lshlrev_b32_e32 v67, 2, v114
	s_waitcnt lgkmcnt(2)
	v_add_f32_e32 v18, v18, v43
	v_or_b32_e32 v89, 2, v71
	v_or_b32_e32 v88, 3, v71
	v_or_b32_e32 v83, 4, v71
	v_or_b32_e32 v82, 5, v71
	v_or_b32_e32 v81, 6, v71
	v_or_b32_e32 v73, 7, v71
	v_or_b32_e32 v66, 8, v71
	v_or_b32_e32 v64, 9, v71
	v_add_f32_e32 v71, v62, v2
	v_add_u32_e32 v2, 0x12bdc, v67
	s_waitcnt lgkmcnt(1)
	v_add_f32_e32 v18, v18, v44
	ds_read_b32 v19, v27 offset:504
	ds_read_u16 v22, v80
	ds_read_u16 v23, v75
	ds_read_u16 v24, v75 offset:80
	ds_read_u16 v25, v75 offset:160
	ds_read_u16 v27, v75 offset:240
	ds_read_u16 v29, v75 offset:320
	ds_read_u16 v33, v75 offset:400
	ds_read_b32 v2, v2
	s_waitcnt lgkmcnt(9)
	v_add_f32_e32 v18, v18, v45
	v_or_b32_e32 v20, 0xb600, v67
	s_movk_i32 s0, 0x540
	s_waitcnt lgkmcnt(8)
	v_add_f32_e32 v42, v18, v19
	v_mad_u64_u32 v[18:19], s[0:1], v65, s0, v[20:21]
	s_movk_i32 s0, 0x54
	s_nop 0
	v_mad_u64_u32 v[20:21], s[8:9], v70, s0, v[20:21]
	ds_read_b32 v19, v20 offset:1176
	s_waitcnt lgkmcnt(1)
	v_add_f32_e32 v2, v42, v2
	v_fmamk_f32 v2, v2, 0x3c064b8a, v69
	v_cvt_f32_f16_e32 v69, v22
	v_max_f32_e32 v2, 0, v2
	v_mul_f32_e32 v2, 0xbfb8aa3b, v2
	v_exp_f32_e32 v2, v2
	v_mul_f32_e32 v21, 0xbfb8aa3b, v69
	v_exp_f32_e32 v22, v21
	v_cvt_f32_f16_e32 v75, v23
	v_add_f32_e32 v2, 1.0, v2
	v_rcp_f32_e32 v21, v2
	v_add_f32_e32 v2, 1.0, v22
	v_rcp_f32_e32 v80, v2
	v_mul_f32_e32 v2, 0xbfb8aa3b, v75
	v_exp_f32_e32 v2, v2
	v_cvt_f32_f16_e32 v91, v24
	v_cvt_f32_f16_e32 v94, v25
	v_cvt_f32_f16_e32 v97, v27
	v_add_f32_e32 v2, 1.0, v2
	v_rcp_f32_e32 v92, v2
	v_mul_f32_e32 v2, 0xbfb8aa3b, v91
	v_exp_f32_e32 v2, v2
	v_fmac_f32_e32 v59, v99, v77
	v_cvt_f32_f16_e32 v100, v29
	v_cvt_f32_f16_e32 v103, v33
	v_add_f32_e32 v2, 1.0, v2
	v_rcp_f32_e32 v95, v2
	v_mul_f32_e32 v2, 0xbfb8aa3b, v94
	v_exp_f32_e32 v2, v2
	ds_read2_b32 v[22:23], v20 offset1:21
	v_add_f32_e32 v90, v62, v3
	v_add_f32_e32 v93, v62, v4
	v_add_f32_e32 v2, 1.0, v2
	v_rcp_f32_e32 v77, v2
	v_mul_f32_e32 v2, 0xbfb8aa3b, v97
	v_exp_f32_e32 v2, v2
	ds_read2_b32 v[24:25], v20 offset0:42 offset1:63
	v_add_f32_e32 v96, v62, v5
	v_add_f32_e32 v98, v62, v6
	v_add_f32_e32 v2, 1.0, v2
	v_rcp_f32_e32 v101, v2
	v_mul_f32_e32 v2, 0xbfb8aa3b, v100
	v_exp_f32_e32 v2, v2
	ds_read2_b32 v[42:43], v20 offset0:84 offset1:105
	v_add_f32_e32 v102, v62, v7
	v_fmac_f32_e32 v72, v99, v79
	v_add_f32_e32 v2, 1.0, v2
	v_rcp_f32_e32 v104, v2
	v_mul_f32_e32 v2, 0xbfb8aa3b, v103
	v_exp_f32_e32 v2, v2
	ds_read_u16 v3, v51
	ds_read_u16 v4, v51 offset:80
	ds_read_u16 v5, v51 offset:160
	ds_read_u16 v6, v51 offset:240
	ds_read_u16 v7, v51 offset:320
	ds_read_u16 v33, v51 offset:400
	ds_read_u16 v79, v51 offset:480
	ds_read_u16 v106, v51 offset:560
	s_waitcnt lgkmcnt(7)
	v_cvt_f32_f16_e32 v107, v3
	s_waitcnt lgkmcnt(6)
	v_cvt_f32_f16_e32 v27, v4
	v_add_f32_e32 v2, 1.0, v2
	v_rcp_f32_e32 v108, v2
	v_mul_f32_e32 v2, 0xbfb8aa3b, v107
	v_exp_f32_e32 v2, v2
	v_fmac_f32_e32 v52, v99, v35
	s_waitcnt lgkmcnt(5)
	v_cvt_f32_f16_e32 v35, v5
	v_fmac_f32_e32 v26, v99, v84
	v_add_f32_e32 v2, 1.0, v2
	v_rcp_f32_e32 v110, v2
	v_mul_f32_e32 v2, 0xbfb8aa3b, v27
	v_exp_f32_e32 v2, v2
	s_waitcnt lgkmcnt(4)
	v_cvt_f32_f16_e32 v29, v6
	v_fmac_f32_e32 v53, v99, v76
	v_add_f32_e32 v76, v62, v11
	v_add_f32_e32 v2, 1.0, v2
	v_rcp_f32_e32 v84, v2
	v_mul_f32_e32 v2, 0xbfb8aa3b, v35
	v_exp_f32_e32 v2, v2
	v_fmac_f32_e32 v58, v99, v37
	s_waitcnt lgkmcnt(3)
	v_cvt_f32_f16_e32 v37, v7
	v_fmac_f32_e32 v60, v99, v39
	v_add_f32_e32 v2, 1.0, v2
	v_rcp_f32_e32 v11, v2
	v_mul_f32_e32 v2, 0xbfb8aa3b, v29
	v_exp_f32_e32 v2, v2
	v_fmac_f32_e32 v74, v99, v41
	s_waitcnt lgkmcnt(2)
	v_cvt_f32_f16_e32 v39, v33
	s_waitcnt lgkmcnt(1)
	v_cvt_f32_f16_e32 v41, v79
	v_add_f32_e32 v2, 1.0, v2
	v_fmac_f32_e32 v34, v99, v85
	v_rcp_f32_e32 v85, v2
	v_mul_f32_e32 v2, 0xbfb8aa3b, v37
	v_exp_f32_e32 v2, v2
	v_mul_f32_e32 v3, 0xbfb8aa3b, v39
	v_mul_f32_e32 v6, 0xbfb8aa3b, v41
	v_exp_f32_e32 v3, v3
	v_exp_f32_e32 v6, v6
	s_waitcnt lgkmcnt(0)
	v_cvt_f32_f16_e32 v33, v106
	v_add_f32_e32 v2, 1.0, v2
	v_add_f32_e32 v46, v62, v13
	v_rcp_f32_e32 v13, v2
	v_add_f32_e32 v2, 1.0, v3
	v_add_f32_e32 v6, 1.0, v6
	v_fmac_f32_e32 v28, v99, v86
	v_fmac_f32_e32 v36, v99, v87
	v_rcp_f32_e32 v86, v2
	v_add_u32_e32 v2, 0x200, v20
	v_rcp_f32_e32 v87, v6
	v_mul_f32_e32 v6, 0xbfb8aa3b, v33
	v_add_f32_e32 v105, v62, v8
	ds_read2_b32 v[44:45], v20 offset0:126 offset1:147
	v_add_f32_e32 v109, v62, v9
	v_add_f32_e32 v70, v62, v10
	ds_read2_b32 v[8:9], v20 offset0:168 offset1:189
	ds_read2_b32 v[4:5], v20 offset0:210 offset1:231
	ds_read2_b32 v[2:3], v2 offset0:124 offset1:145
	v_add_f32_e32 v10, v62, v15
	v_exp_f32_e32 v6, v6
	ds_read_b32 v15, v18
	ds_read_u16 v7, v51 offset:640
	v_mov_b32_e32 v20, v17
	v_fmac_f32_e32 v40, v99, v31
	v_add_f32_e32 v6, 1.0, v6
	v_rcp_f32_e32 v18, v6
	s_waitcnt lgkmcnt(0)
	v_cvt_f32_f16_e32 v31, v7
	v_pk_add_f32 v[6:7], v[62:63], v[20:21]
	v_fmac_f32_e32 v61, v99, v78
	v_add_f32_e32 v78, v62, v12
	v_add_f32_e32 v12, v62, v16
	v_mul_f32_e32 v16, v7, v69
	v_fmac_f32_e32 v16, v71, v52
	v_fmac_f32_e32 v15, v16, v80
	v_mul_f32_e32 v16, v7, v75
	v_fmac_f32_e32 v16, v90, v53
	v_add_f32_e32 v15, 0, v15
	v_fma_f32 v16, v16, v92, v22
	v_add_f32_e32 v15, v15, v16
	v_mul_f32_e32 v16, v7, v91
	s_movk_i32 s1, 0x7a
	v_fmac_f32_e32 v16, v93, v58
	v_fmac_f32_e32 v23, v16, v95
	v_cmp_gt_u32_e32 vcc, s1, v89
	v_mov_b32_e32 v71, v7
	v_mov_b32_e32 v79, v7
	v_cndmask_b32_e32 v16, 0, v23, vcc
	v_add_f32_e32 v15, v15, v16
	v_mul_f32_e32 v16, v7, v94
	v_fmac_f32_e32 v16, v96, v59
	v_fma_f32 v16, v16, v77, v24
	v_cmp_gt_u32_e32 vcc, s1, v88
	v_mov_b32_e32 v77, v7
	v_fmac_f32_e32 v38, v99, v47
	v_cndmask_b32_e32 v16, 0, v16, vcc
	v_add_f32_e32 v15, v15, v16
	v_mul_f32_e32 v16, v7, v97
	v_fmac_f32_e32 v16, v98, v60
	v_fmac_f32_e32 v25, v16, v101
	v_cmp_gt_u32_e32 vcc, s1, v83
	v_mov_b32_e32 v47, v7
	v_add_f32_e32 v14, v62, v14
	v_cndmask_b32_e32 v16, 0, v25, vcc
	v_add_f32_e32 v15, v15, v16
	v_mul_f32_e32 v16, v7, v100
	v_fmac_f32_e32 v16, v102, v61
	v_fma_f32 v16, v16, v104, v42
	v_cmp_gt_u32_e32 vcc, s1, v82
	v_fmac_f32_e32 v32, v99, v48
	v_fmac_f32_e32 v30, v99, v49
	v_cndmask_b32_e32 v16, 0, v16, vcc
	v_add_f32_e32 v15, v15, v16
	v_mul_f32_e32 v16, v7, v103
	v_fmac_f32_e32 v16, v105, v72
	v_fmac_f32_e32 v43, v16, v108
	v_cmp_gt_u32_e32 vcc, s1, v81
	s_nop 1
	v_cndmask_b32_e32 v16, 0, v43, vcc
	v_add_f32_e32 v15, v15, v16
	v_mul_f32_e32 v16, v7, v107
	v_fmac_f32_e32 v16, v109, v74
	v_fma_f32 v16, v16, v110, v44
	v_cmp_gt_u32_e32 vcc, s1, v73
	s_nop 1
	v_cndmask_b32_e32 v16, 0, v16, vcc
	v_add_f32_e32 v15, v15, v16
	v_pk_mul_f32 v[16:17], v[70:71], v[26:27]
	v_cmp_gt_u32_e32 vcc, s1, v66
	v_add_f32_e32 v16, v16, v17
	v_fmac_f32_e32 v45, v16, v84
	v_cndmask_b32_e32 v16, 0, v45, vcc
	v_add_f32_e32 v15, v15, v16
	v_pk_mul_f32 v[16:17], v[76:77], v[34:35]
	v_cmp_gt_u32_e32 vcc, s1, v64
	v_add_f32_e32 v16, v16, v17
	v_fma_f32 v8, v16, v11, v8
	v_pk_mul_f32 v[16:17], v[78:79], v[28:29]
	v_cndmask_b32_e32 v8, 0, v8, vcc
	v_add_f32_e32 v11, v16, v17
	v_fmac_f32_e32 v9, v11, v85
	v_cmp_gt_u32_e32 vcc, s1, v68
	v_add_f32_e32 v8, v15, v8
	v_mov_b32_e32 v15, v7
	v_cndmask_b32_e32 v9, 0, v9, vcc
	v_add_f32_e32 v11, v8, v9
	v_pk_mul_f32 v[8:9], v[46:47], v[36:37]
	v_cmp_gt_u32_e32 vcc, s1, v57
	v_add_f32_e32 v8, v8, v9
	v_fma_f32 v4, v8, v13, v4
	v_pk_mul_f32 v[8:9], v[14:15], v[38:39]
	v_cndmask_b32_e32 v4, 0, v4, vcc
	v_add_f32_e32 v8, v8, v9
	v_fmac_f32_e32 v5, v8, v86
	v_cmp_gt_u32_e32 vcc, s1, v56
	v_add_f32_e32 v4, v11, v4
	v_mov_b32_e32 v11, v7
	v_cndmask_b32_e32 v5, 0, v5, vcc
	v_add_f32_e32 v8, v4, v5
	v_pk_mul_f32 v[4:5], v[10:11], v[40:41]
	v_mov_b32_e32 v13, v7
	v_add_f32_e32 v4, v4, v5
	v_fma_f32 v2, v4, v87, v2
	v_pk_mul_f32 v[4:5], v[12:13], v[32:33]
	v_cmp_gt_u32_e32 vcc, s1, v55
	v_add_f32_e32 v4, v4, v5
	v_mul_f32_e32 v5, 0xbfb8aa3b, v31
	v_exp_f32_e32 v5, v5
	v_fmac_f32_e32 v3, v4, v18
	v_cndmask_b32_e32 v2, 0, v2, vcc
	v_cmp_gt_u32_e32 vcc, s1, v54
	v_add_f32_e32 v4, 1.0, v5
	v_rcp_f32_e32 v4, v4
	v_add_f32_e32 v2, v8, v2
	v_cndmask_b32_e32 v3, 0, v3, vcc
	v_add_f32_e32 v5, v2, v3
	v_pk_mul_f32 v[2:3], v[6:7], v[30:31]
	v_cmp_gt_u32_e32 vcc, s1, v50
	v_add_f32_e32 v2, v2, v3
	v_fmac_f32_e32 v19, v2, v4
	v_cndmask_b32_e32 v2, 0, v19, vcc
	v_mul_lo_u32 v3, v65, s0
	s_mov_b32 s0, 0x12c30
	v_add_f32_e32 v2, v5, v2
	v_add3_u32 v3, v3, v67, s0
	ds_write_b32 v3, v2

	.amdhsa_kernel _Z6k_mainPKfPKDv8_DF16_S0_S3_S0_S0_S0_S0_S0_S0_S0_S0_S0_S3_S0_S0_S0_S0_S0_S0_S0_S0_S0_S0_S0_S0_S0_Pf
		.amdhsa_group_segment_fixed_size 78032
		.amdhsa_private_segment_fixed_size 0
		.amdhsa_kernarg_size 224
		.amdhsa_user_sgpr_count 2
		.amdhsa_user_sgpr_dispatch_ptr 0
		.amdhsa_user_sgpr_queue_ptr 0
		.amdhsa_user_sgpr_kernarg_segment_ptr 1
		.amdhsa_user_sgpr_dispatch_id 0
		.amdhsa_user_sgpr_kernarg_preload_length 0
		.amdhsa_user_sgpr_kernarg_preload_offset 0
		.amdhsa_user_sgpr_private_segment_size 0
		.amdhsa_uses_dynamic_stack 0
		.amdhsa_enable_private_segment 0
		.amdhsa_system_sgpr_workgroup_id_x 1
		.amdhsa_system_sgpr_workgroup_id_y 0
		.amdhsa_system_sgpr_workgroup_id_z 0
		.amdhsa_system_sgpr_workgroup_info 0
		.amdhsa_system_vgpr_workitem_id 0
		.amdhsa_next_free_vgpr 128
		.amdhsa_next_free_sgpr 96
		.amdhsa_accum_offset 128
		.amdhsa_reserve_vcc 1
		.amdhsa_float_round_mode_32 0
		.amdhsa_float_round_mode_16_64 0
		.amdhsa_float_denorm_mode_32 3
		.amdhsa_float_denorm_mode_16_64 3
		.amdhsa_dx10_clamp 1
		.amdhsa_ieee_mode 1
		.amdhsa_fp16_overflow 0
		.amdhsa_tg_split 0
		.amdhsa_exception_fp_ieee_invalid_op 0
		.amdhsa_exception_fp_denorm_src 0
		.amdhsa_exception_fp_ieee_div_zero 0
		.amdhsa_exception_fp_ieee_overflow 0
		.amdhsa_exception_fp_ieee_underflow 0
		.amdhsa_exception_fp_ieee_inexact 0
		.amdhsa_exception_int_div_zero 0
	.end_amdhsa_kernel

amdhsa.kernels:
  - .agpr_count:     0
    .args:
      - .actual_access:  read_only
        .address_space:  global
        .offset:         0
        .size:           8
        .value_kind:     global_buffer
      - .actual_access:  read_only
        .address_space:  global
        .offset:         8
        .size:           8
        .value_kind:     global_buffer
      - .actual_access:  read_only
        .address_space:  global
        .offset:         16
        .size:           8
        .value_kind:     global_buffer
      - .actual_access:  read_only
        .address_space:  global
        .offset:         24
        .size:           8
        .value_kind:     global_buffer
      - .actual_access:  read_only
        .address_space:  global
        .offset:         32
        .size:           8
        .value_kind:     global_buffer
      - .actual_access:  read_only
        .address_space:  global
        .offset:         40
        .size:           8
        .value_kind:     global_buffer
      - .actual_access:  read_only
        .address_space:  global
        .offset:         48
        .size:           8
        .value_kind:     global_buffer
      - .actual_access:  read_only
        .address_space:  global
        .offset:         56
        .size:           8
        .value_kind:     global_buffer
      - .actual_access:  read_only
        .address_space:  global
        .offset:         64
        .size:           8
        .value_kind:     global_buffer
      - .actual_access:  read_only
        .address_space:  global
        .offset:         72
        .size:           8
        .value_kind:     global_buffer
      - .actual_access:  read_only
        .address_space:  global
        .offset:         80
        .size:           8
        .value_kind:     global_buffer
      - .actual_access:  read_only
        .address_space:  global
        .offset:         88
        .size:           8
        .value_kind:     global_buffer
      - .actual_access:  read_only
        .address_space:  global
        .offset:         96
        .size:           8
        .value_kind:     global_buffer
      - .address_space:  global
        .offset:         104
        .size:           8
        .value_kind:     global_buffer
      - .address_space:  global
        .offset:         112
        .size:           8
        .value_kind:     global_buffer
      - .address_space:  global
        .offset:         120
        .size:           8
        .value_kind:     global_buffer
      - .address_space:  global
        .offset:         128
        .size:           8
        .value_kind:     global_buffer
      - .actual_access:  read_only
        .address_space:  global
        .offset:         136
        .size:           8
        .value_kind:     global_buffer
    .group_segment_fixed_size: 0
    .kernarg_segment_align: 8
    .kernarg_segment_size: 144
    .language:       OpenCL C
    .language_version:
      - 2
      - 0
    .max_flat_workgroup_size: 64
    .name:           _Z6k_prepPKfS0_S0_S0_S0_S0_S0_S0_S0_S0_S0_S0_S0_PDv8_DF16_S2_S2_PfS0_
    .private_segment_fixed_size: 0
    .sgpr_count:     38
    .sgpr_spill_count: 0
    .symbol:         _Z6k_prepPKfS0_S0_S0_S0_S0_S0_S0_S0_S0_S0_S0_S0_PDv8_DF16_S2_S2_PfS0_.kd
    .uniform_work_group_size: 1
    .uses_dynamic_stack: false
    .vgpr_count:     51
    .vgpr_spill_count: 0
    .wavefront_size: 64
  - .agpr_count:     0
    .args:
      - .actual_access:  read_only
        .address_space:  global
        .offset:         0
        .size:           8
        .value_kind:     global_buffer
      - .address_space:  global
        .offset:         8
        .size:           8
        .value_kind:     global_buffer
      - .address_space:  global
        .offset:         16
        .size:           8
        .value_kind:     global_buffer
      - .address_space:  global
        .offset:         24
        .size:           8
        .value_kind:     global_buffer
      - .actual_access:  read_only
        .address_space:  global
        .offset:         32
        .size:           8
        .value_kind:     global_buffer
      - .actual_access:  read_only
        .address_space:  global
        .offset:         40
        .size:           8
        .value_kind:     global_buffer
      - .actual_access:  read_only
        .address_space:  global
        .offset:         48
        .size:           8
        .value_kind:     global_buffer
      - .actual_access:  read_only
        .address_space:  global
        .offset:         56
        .size:           8
        .value_kind:     global_buffer
      - .actual_access:  read_only
        .address_space:  global
        .offset:         64
        .size:           8
        .value_kind:     global_buffer
      - .actual_access:  read_only
        .address_space:  global
        .offset:         72
        .size:           8
        .value_kind:     global_buffer
      - .actual_access:  read_only
        .address_space:  global
        .offset:         80
        .size:           8
        .value_kind:     global_buffer
      - .actual_access:  read_only
        .address_space:  global
        .offset:         88
        .size:           8
        .value_kind:     global_buffer
      - .actual_access:  read_only
        .address_space:  global
        .offset:         96
        .size:           8
        .value_kind:     global_buffer
      - .address_space:  global
        .offset:         104
        .size:           8
        .value_kind:     global_buffer
      - .actual_access:  read_only
        .address_space:  global
        .offset:         112
        .size:           8
        .value_kind:     global_buffer
      - .actual_access:  read_only
        .address_space:  global
        .offset:         120
        .size:           8
        .value_kind:     global_buffer
      - .actual_access:  read_only
        .address_space:  global
        .offset:         128
        .size:           8
        .value_kind:     global_buffer
      - .actual_access:  read_only
        .address_space:  global
        .offset:         136
        .size:           8
        .value_kind:     global_buffer
      - .actual_access:  read_only
        .address_space:  global
        .offset:         144
        .size:           8
        .value_kind:     global_buffer
      - .actual_access:  read_only
        .address_space:  global
        .offset:         152
        .size:           8
        .value_kind:     global_buffer
      - .actual_access:  read_only
        .address_space:  global
        .offset:         160
        .size:           8
        .value_kind:     global_buffer
      - .actual_access:  read_only
        .address_space:  global
        .offset:         168
        .size:           8
        .value_kind:     global_buffer
      - .actual_access:  read_only
        .address_space:  global
        .offset:         176
        .size:           8
        .value_kind:     global_buffer
      - .actual_access:  read_only
        .address_space:  global
        .offset:         184
        .size:           8
        .value_kind:     global_buffer
      - .actual_access:  read_only
        .address_space:  global
        .offset:         192
        .size:           8
        .value_kind:     global_buffer
      - .actual_access:  read_only
        .address_space:  global
        .offset:         200
        .size:           8
        .value_kind:     global_buffer
      - .actual_access:  read_only
        .address_space:  global
        .offset:         208
        .size:           8
        .value_kind:     global_buffer
      - .actual_access:  write_only
        .address_space:  global
        .offset:         216
        .size:           8
        .value_kind:     global_buffer
    .group_segment_fixed_size: 78032
    .kernarg_segment_align: 8
    .kernarg_segment_size: 224
    .language:       OpenCL C
    .language_version:
      - 2
      - 0
    .max_flat_workgroup_size: 512
    .name:           _Z6k_mainPKfPKDv8_DF16_S0_S3_S0_S0_S0_S0_S0_S0_S0_S0_S0_S3_S0_S0_S0_S0_S0_S0_S0_S0_S0_S0_S0_S0_S0_Pf
    .private_segment_fixed_size: 0
    .sgpr_count:     78
    .sgpr_spill_count: 0
    .symbol:         _Z6k_mainPKfPKDv8_DF16_S0_S3_S0_S0_S0_S0_S0_S0_S0_S0_S0_S3_S0_S0_S0_S0_S0_S0_S0_S0_S0_S0_S0_S0_S0_Pf.kd
    .uniform_work_group_size: 1
    .uses_dynamic_stack: false
    .vgpr_count:     128
    .vgpr_spill_count: 0
    .wavefront_size: 64
